# speedup vs baseline: 1.0234x; 1.0113x over previous
_Z6k_gramILi0EEvPK15HIP_vector_typeIjLj4EEPyPf:
	s_load_dwordx4 s[8:11], s[0:1], 0x0
	s_load_dwordx2 s[4:5], s[0:1], 0x10
	s_lshl_b32 s0, s2, 2
	s_and_b32 s0, s0, 28
	s_ashr_i32 s1, s2, 6
	s_add_i32 s16, s0, s1
	v_readfirstlane_b32 s23, v0
	s_ashr_i32 s17, s16, 31
	s_lshr_b32 s21, s23, 6
	s_bfe_u32 s18, s23, 0x20006
	s_lshr_b32 s22, s2, 3
	s_bfe_u32 s20, s2, 0x30003
	s_lshl_b64 s[0:1], s[16:17], 20
	s_waitcnt lgkmcnt(0)
	s_add_u32 s12, s8, s0
	v_mov_b32_e32 v1, 0x20000
	s_addc_u32 s0, s9, s1
	s_lshl_b32 s1, s20, 2
	v_lshl_or_b32 v1, v0, 2, v1
	v_bfrev_b32_e32 v2, 1
	s_cmp_lt_u32 s20, 4
	ds_write_b32 v1, v2
	s_mov_b32 s24, 4
	s_mov_b32 s15, 0x20000
	s_and_b32 s13, s0, 0xffff
	s_mov_b32 s14, 0x100000
	v_lshlrev_b32_e32 v166, 4, v0
	s_lshl_b32 s25, s21, 10
	s_lshl_b32 s0, s20, 17
	s_mov_b32 m0, s25
	s_nop 0
	buffer_load_dwordx4 v166, s[12:15], s0 offen lds
	s_add_i32 s26, s25, 0x2000
	s_or_b32 s2, s0, 0x2000
	s_mov_b32 m0, s26
	s_nop 0
	buffer_load_dwordx4 v166, s[12:15], s2 offen lds
	s_add_i32 s27, s25, 0x4000
	s_or_b32 s2, s0, 0x8000
	s_mov_b32 m0, s27
	s_nop 0
	buffer_load_dwordx4 v166, s[12:15], s2 offen lds
	s_add_i32 s28, s25, 0x6000
	s_or_b32 s2, s0, 0xa000
	s_mov_b32 m0, s28
	s_nop 0
	buffer_load_dwordx4 v166, s[12:15], s2 offen lds
	s_add_i32 s34, s25, 0x10000
	s_or_b32 s2, s0, 0x10000
	s_mov_b32 m0, s34
	s_nop 0
	buffer_load_dwordx4 v166, s[12:15], s2 offen lds
	s_add_i32 s35, s25, 0x12000
	s_or_b32 s2, s0, 0x12000
	s_mov_b32 m0, s35
	s_nop 0
	buffer_load_dwordx4 v166, s[12:15], s2 offen lds
	s_add_i32 s36, s25, 0x14000
	s_or_b32 s2, s0, 0x18000
	s_mov_b32 m0, s36
	s_nop 0
	buffer_load_dwordx4 v166, s[12:15], s2 offen lds
	s_add_i32 s37, s25, 0x16000
	s_or_b32 s2, s0, 0x1a000
	s_mov_b32 m0, s37
	s_nop 0
	buffer_load_dwordx4 v166, s[12:15], s2 offen lds
	s_add_i32 s29, s25, 0x8000
	s_or_b32 s2, s0, 0x4000
	s_mov_b32 m0, s29
	s_nop 0
	buffer_load_dwordx4 v166, s[12:15], s2 offen lds
	s_add_i32 s30, s25, 0xa000
	s_or_b32 s2, s0, 0x6000
	s_mov_b32 m0, s30
	s_nop 0
	buffer_load_dwordx4 v166, s[12:15], s2 offen lds
	s_add_i32 s31, s25, 0xc000
	s_or_b32 s2, s0, 0xc000
	s_mov_b32 m0, s31
	s_nop 0
	buffer_load_dwordx4 v166, s[12:15], s2 offen lds
	s_add_i32 s33, s25, 0xe000
	s_or_b32 s2, s0, 0xe000
	s_mov_b32 m0, s33
	s_nop 0
	buffer_load_dwordx4 v166, s[12:15], s2 offen lds
	s_add_i32 s38, s25, 0x18000
	s_or_b32 s2, s0, 0x14000
	s_mov_b32 m0, s38
	s_nop 0
	buffer_load_dwordx4 v166, s[12:15], s2 offen lds
	s_add_i32 s39, s25, 0x1a000
	s_or_b32 s2, s0, 0x16000
	s_mov_b32 m0, s39
	s_nop 0
	buffer_load_dwordx4 v166, s[12:15], s2 offen lds
	s_add_i32 s40, s25, 0x1c000
	s_or_b32 s2, s0, 0x1c000
	s_mov_b32 m0, s40
	s_nop 0
	buffer_load_dwordx4 v166, s[12:15], s2 offen lds
	s_add_i32 s42, s25, 0x1e000
	s_or_b32 s2, s0, 0x1e000
	s_mov_b32 m0, s42
	s_nop 0
	buffer_load_dwordx4 v166, s[12:15], s2 offen lds
	s_lshl_b32 s0, s23, 9
	s_lshl_b32 s2, s23, 8
	v_and_b32_e32 v167, 15, v0
	v_bfe_u32 v160, v0, 4, 2
	s_and_b32 s0, s0, 0x10000
	s_and_b32 s2, s2, 0x4000
	v_lshlrev_b32_e32 v128, 9, v160
	v_lshlrev_b32_e32 v129, 4, v167
	s_or_b32 s0, s0, s2
	v_or3_b32 v124, s0, v128, v129
	s_waitcnt vmcnt(8)
	s_waitcnt lgkmcnt(0)
	s_barrier
	ds_read_b128 v[0:3], v124
	ds_read_b128 v[4:7], v124 offset:256
	ds_read_b128 v[8:11], v124 offset:2048
	ds_read_b128 v[12:15], v124 offset:2304
	ds_read_b128 v[16:19], v124 offset:4096
	ds_read_b128 v[20:23], v124 offset:4352
	ds_read_b128 v[24:27], v124 offset:6144
	ds_read_b128 v[28:31], v124 offset:6400
	ds_read_b128 v[32:35], v124 offset:8192
	ds_read_b128 v[36:39], v124 offset:8448
	ds_read_b128 v[40:43], v124 offset:10240
	ds_read_b128 v[44:47], v124 offset:10496
	ds_read_b128 v[48:51], v124 offset:12288
	ds_read_b128 v[52:55], v124 offset:12544
	ds_read_b128 v[56:59], v124 offset:14336
	ds_read_b128 v[60:63], v124 offset:14592
	s_lshr_b32 s41, s23, 8
	s_lshl_b32 s0, s41, 14
	s_lshl_b32 s50, s24, 2
	v_or3_b32 v168, s0, v128, v129
	s_or_b32 s43, s18, s1
	s_lshl_b32 s0, s16, 10
	s_lshl_b32 s1, s43, 5
	ds_read_b128 v[128:131], v168
	ds_read_b128 v[132:135], v168 offset:256
	ds_read_b128 v[136:139], v168 offset:2048
	ds_read_b128 v[140:143], v168 offset:2304
	s_or_b32 s0, s1, s0
	v_or_b32_e32 v144, s0, v167
	v_lshlrev_b32_e32 v146, 2, v160
	v_ashrrev_i32_e32 v145, 31, v144
	v_lshl_add_u64 v[164:165], v[144:145], 2, s[4:5]
	v_or_b32_e32 v144, 1, v146
	v_cmp_eq_u32_e64 s[2:3], v144, v167
	v_or_b32_e32 v144, 2, v146
	s_waitcnt vmcnt(8)
	v_cmp_eq_u32_e64 s[4:5], v144, v167
	v_or_b32_e32 v144, 3, v146
	s_add_i32 s44, s50, 3
	s_lshl_b32 s45, s22, 2
	v_cmp_eq_u32_e64 s[0:1], v146, v167
	v_cmp_eq_u32_e64 s[6:7], v144, v167
	v_add_u32_e32 v169, 0x10000, v168
	v_add_u32_e32 v170, 0x10100, v168
	v_add_u32_e32 v171, 0x10800, v168
	v_add_u32_e32 v172, 0x10900, v168
	s_barrier
	s_add_i32 s8, s45, 28
	s_and_b32 s8, s8, 28
	s_add_i32 s8, s41, s8
	s_lshl_b32 s8, s8, 1
	s_add_i32 s9, s8, 4
	s_add_i32 s8, s8, 5
	v_mov_b32_e32 v148, s9
	v_mov_b32_e32 v149, s8
	ds_read_b128 v[148:151], v168 offset:4096
	s_waitcnt lgkmcnt(4)
	v_mfma_f32_16x16x32_bf16 v[144:147], v[0:3], v[128:131], 0
	v_mfma_f32_16x16x32_bf16 v[128:131], v[4:7], v[128:131], 0
	ds_read_b128 v[156:159], v168 offset:4352
	s_waitcnt lgkmcnt(4)
	v_mfma_f32_16x16x32_bf16 v[152:155], v[0:3], v[132:135], 0
	v_mfma_f32_16x16x32_bf16 v[132:135], v[4:7], v[132:135], 0
	s_waitcnt lgkmcnt(3)
	v_mfma_f32_16x16x32_bf16 v[144:147], v[8:11], v[136:139], v[144:147]
	ds_read_b128 v[174:177], v168 offset:6144
	v_mfma_f32_16x16x32_bf16 v[128:131], v[12:15], v[136:139], v[128:131]
	s_waitcnt lgkmcnt(3)
	v_mfma_f32_16x16x32_bf16 v[136:139], v[8:11], v[140:143], v[152:155]
	s_nop 2
	ds_read_b128 v[152:155], v168 offset:6400
	v_mfma_f32_16x16x32_bf16 v[132:135], v[12:15], v[140:143], v[132:135]
	s_waitcnt lgkmcnt(3)
	v_mfma_f32_16x16x32_bf16 v[140:143], v[16:19], v[148:151], v[144:147]
	s_nop 2
	ds_read_b128 v[144:147], v168 offset:8192
	v_mfma_f32_16x16x32_bf16 v[128:131], v[20:23], v[148:151], v[128:131]
	ds_read_b128 v[148:151], v168 offset:8448
	s_waitcnt lgkmcnt(4)
	v_mfma_f32_16x16x32_bf16 v[136:139], v[16:19], v[156:159], v[136:139]
	v_mfma_f32_16x16x32_bf16 v[132:135], v[20:23], v[156:159], v[132:135]
	ds_read_b128 v[156:159], v168 offset:10240
	s_waitcnt lgkmcnt(4)
	v_mfma_f32_16x16x32_bf16 v[140:143], v[24:27], v[174:177], v[140:143]
	v_mfma_f32_16x16x32_bf16 v[128:131], v[28:31], v[174:177], v[128:131]
	s_waitcnt lgkmcnt(3)
	v_mfma_f32_16x16x32_bf16 v[136:139], v[24:27], v[152:155], v[136:139]
	ds_read_b128 v[174:177], v168 offset:10496
	v_mfma_f32_16x16x32_bf16 v[132:135], v[28:31], v[152:155], v[132:135]
	ds_read_b128 v[152:155], v168 offset:12288
	s_waitcnt lgkmcnt(4)
	v_mfma_f32_16x16x32_bf16 v[140:143], v[32:35], v[144:147], v[140:143]
	v_mfma_f32_16x16x32_bf16 v[128:131], v[36:39], v[144:147], v[128:131]
	ds_read_b128 v[144:147], v168 offset:12544
	s_waitcnt lgkmcnt(4)
	v_mfma_f32_16x16x32_bf16 v[136:139], v[32:35], v[148:151], v[136:139]
	v_mfma_f32_16x16x32_bf16 v[132:135], v[36:39], v[148:151], v[132:135]
	ds_read_b128 v[148:151], v168 offset:14336
	s_waitcnt lgkmcnt(4)
	v_mfma_f32_16x16x32_bf16 v[140:143], v[40:43], v[156:159], v[140:143]
	v_mfma_f32_16x16x32_bf16 v[128:131], v[44:47], v[156:159], v[128:131]
	ds_read_b128 v[156:159], v168 offset:14592
	s_waitcnt lgkmcnt(4)
	v_mfma_f32_16x16x32_bf16 v[136:139], v[40:43], v[174:177], v[136:139]
	v_mfma_f32_16x16x32_bf16 v[132:135], v[44:47], v[174:177], v[132:135]
	s_waitcnt lgkmcnt(3)
	v_mfma_f32_16x16x32_bf16 v[140:143], v[48:51], v[152:155], v[140:143]
	ds_read_b128 v[174:177], v168 offset:32768
	v_mfma_f32_16x16x32_bf16 v[128:131], v[52:55], v[152:155], v[128:131]
	ds_read_b128 v[152:155], v168 offset:33024
	s_waitcnt lgkmcnt(4)
	v_mfma_f32_16x16x32_bf16 v[136:139], v[48:51], v[144:147], v[136:139]
	v_mfma_f32_16x16x32_bf16 v[132:135], v[52:55], v[144:147], v[132:135]
	ds_read_b128 v[144:147], v168 offset:34816
	s_waitcnt lgkmcnt(4)
	v_mfma_f32_16x16x32_bf16 v[140:143], v[56:59], v[148:151], v[140:143]
	v_mfma_f32_16x16x32_bf16 v[128:131], v[60:63], v[148:151], v[128:131]
	ds_read_b128 v[148:151], v168 offset:35072
	s_waitcnt lgkmcnt(4)
	v_mfma_f32_16x16x32_bf16 v[136:139], v[56:59], v[156:159], v[136:139]
	v_mfma_f32_16x16x32_bf16 v[132:135], v[60:63], v[156:159], v[132:135]
	s_waitcnt vmcnt(0)
	s_barrier
	ds_read_b128 v[64:67], v124 offset:32768
	ds_read_b128 v[68:71], v124 offset:33024
	ds_read_b128 v[72:75], v124 offset:34816
	ds_read_b128 v[76:79], v124 offset:35072
	ds_read_b128 v[80:83], v124 offset:36864
	ds_read_b128 v[84:87], v124 offset:37120
	ds_read_b128 v[88:91], v124 offset:38912
	ds_read_b128 v[92:95], v124 offset:39168
	ds_read_b128 v[96:99], v124 offset:40960
	ds_read_b128 v[100:103], v124 offset:41216
	ds_read_b128 v[104:107], v124 offset:43008
	ds_read_b128 v[108:111], v124 offset:43264
	ds_read_b128 v[112:115], v124 offset:45056
	ds_read_b128 v[116:119], v124 offset:45312
	ds_read_b128 v[120:123], v124 offset:47104
	ds_read_b128 v[124:127], v124 offset:47360
	ds_read_b128 v[174:177], v168 offset:32768
	ds_read_b128 v[152:155], v168 offset:33024
	ds_read_b128 v[144:147], v168 offset:34816
	ds_read_b128 v[148:151], v168 offset:35072
	s_waitcnt lgkmcnt(0)
	s_and_b32 s8, s45, 28
	s_add_i32 s8, s8, s41
	s_lshl_b32 s19, s8, 1
	s_or_b32 s51, s19, 1
	v_mov_b32_e32 v156, s51
	v_mov_b32_e32 v157, s19
	ds_read_b128 v[156:159], v168 offset:36864
	s_waitcnt lgkmcnt(4)
	v_mfma_f32_16x16x32_bf16 v[140:143], v[64:67], v[174:177], v[140:143]
	s_min_u32 s9, s44, 4
	s_add_i32 s46, s9, s45
	v_mov_b32_e32 v202, s19
	v_mfma_f32_16x16x32_bf16 v[128:131], v[68:71], v[174:177], v[128:131]
	v_mov_b32_e32 v206, s51
	s_and_b32 s46, s46, 28
	s_and_b32 s47, s9, 2
	s_lshl_b32 s9, s9, 14
	s_or_b32 s46, s47, s46
	s_and_b32 s9, s9, 0x4000
	ds_read_b128 v[174:177], v168 offset:37120
	s_waitcnt lgkmcnt(4)
	v_mfma_f32_16x16x32_bf16 v[136:139], v[64:67], v[152:155], v[136:139]
	s_lshl_b32 s46, s46, 15
	s_or_b32 s9, s46, s9
	s_mov_b32 m0, s25
	s_nop 0
	buffer_load_dwordx4 v166, s[12:15], s9 offen lds
	v_mfma_f32_16x16x32_bf16 v[132:135], v[68:71], v[152:155], v[132:135]
	ds_read_b128 v[152:155], v168 offset:38912
	s_waitcnt lgkmcnt(4)
	v_mfma_f32_16x16x32_bf16 v[140:143], v[72:75], v[144:147], v[140:143]
	v_mfma_f32_16x16x32_bf16 v[128:131], v[76:79], v[144:147], v[128:131]
	ds_read_b128 v[144:147], v168 offset:39168
	s_waitcnt lgkmcnt(4)
	v_mfma_f32_16x16x32_bf16 v[136:139], v[72:75], v[148:151], v[136:139]
	v_mfma_f32_16x16x32_bf16 v[132:135], v[76:79], v[148:151], v[132:135]
	ds_read_b128 v[148:151], v168 offset:40960
	s_waitcnt lgkmcnt(4)
	v_mfma_f32_16x16x32_bf16 v[140:143], v[80:83], v[156:159], v[140:143]
	v_mfma_f32_16x16x32_bf16 v[128:131], v[84:87], v[156:159], v[128:131]
	ds_read_b128 v[156:159], v168 offset:41216
	s_waitcnt lgkmcnt(4)
	v_mfma_f32_16x16x32_bf16 v[136:139], v[80:83], v[174:177], v[136:139]
	s_or_b32 s46, s9, 0x2000
	s_mov_b32 m0, s26
	s_nop 0
	buffer_load_dwordx4 v166, s[12:15], s46 offen lds
	v_mfma_f32_16x16x32_bf16 v[132:135], v[84:87], v[174:177], v[132:135]
	s_waitcnt lgkmcnt(3)
	v_mfma_f32_16x16x32_bf16 v[140:143], v[88:91], v[152:155], v[140:143]
	ds_read_b128 v[174:177], v168 offset:43008
	v_mfma_f32_16x16x32_bf16 v[128:131], v[92:95], v[152:155], v[128:131]
	ds_read_b128 v[152:155], v168 offset:43264
	s_waitcnt lgkmcnt(4)
	v_mfma_f32_16x16x32_bf16 v[136:139], v[88:91], v[144:147], v[136:139]
	v_mfma_f32_16x16x32_bf16 v[132:135], v[92:95], v[144:147], v[132:135]
	ds_read_b128 v[144:147], v168 offset:45056
	s_waitcnt lgkmcnt(4)
	v_mfma_f32_16x16x32_bf16 v[140:143], v[96:99], v[148:151], v[140:143]
	v_mfma_f32_16x16x32_bf16 v[128:131], v[100:103], v[148:151], v[128:131]
	ds_read_b128 v[148:151], v168 offset:45312
	s_waitcnt lgkmcnt(4)
	v_mfma_f32_16x16x32_bf16 v[136:139], v[96:99], v[156:159], v[136:139]
	s_or_b32 s46, s9, 0x8000
	s_mov_b32 m0, s27
	s_nop 0
	buffer_load_dwordx4 v166, s[12:15], s46 offen lds
	v_mfma_f32_16x16x32_bf16 v[132:135], v[100:103], v[156:159], v[132:135]
	s_waitcnt lgkmcnt(3)
	v_mfma_f32_16x16x32_bf16 v[140:143], v[104:107], v[174:177], v[140:143]
	ds_read_b128 v[178:181], v168 offset:47104
	v_mfma_f32_16x16x32_bf16 v[128:131], v[108:111], v[174:177], v[128:131]
	s_waitcnt lgkmcnt(3)
	v_mfma_f32_16x16x32_bf16 v[136:139], v[104:107], v[152:155], v[136:139]
	ds_read_b128 v[174:177], v168 offset:47360
	v_mfma_f32_16x16x32_bf16 v[132:135], v[108:111], v[152:155], v[132:135]
	ds_read_b128 v[156:159], v169
	s_waitcnt lgkmcnt(4)
	v_mfma_f32_16x16x32_bf16 v[140:143], v[112:115], v[144:147], v[140:143]
	v_mfma_f32_16x16x32_bf16 v[128:131], v[116:119], v[144:147], v[128:131]
	ds_read_b128 v[152:155], v170
	s_waitcnt lgkmcnt(4)
	v_mfma_f32_16x16x32_bf16 v[144:147], v[112:115], v[148:151], v[136:139]
	s_or_b32 s9, s9, 0xa000
	s_mov_b32 m0, s28
	s_nop 0
	buffer_load_dwordx4 v166, s[12:15], s9 offen lds
	v_mfma_f32_16x16x32_bf16 v[132:135], v[116:119], v[148:151], v[132:135]
	ds_read_b128 v[148:151], v171
	s_waitcnt lgkmcnt(4)
	v_mfma_f32_16x16x32_bf16 v[136:139], v[120:123], v[178:181], v[140:143]
	v_mfma_f32_16x16x32_bf16 v[128:131], v[124:127], v[178:181], v[128:131]
	s_waitcnt lgkmcnt(3)
	v_mfma_f32_16x16x32_bf16 v[140:143], v[120:123], v[174:177], v[144:147]
	s_nop 2
	ds_read_b128 v[144:147], v172
	v_mfma_f32_16x16x32_bf16 v[132:135], v[124:127], v[174:177], v[132:135]
	s_waitcnt vmcnt(4)
	s_barrier
	s_cmp_lg_u32 s8, s43
	s_cbranch_scc1 .LBB3_11
	s_and_saveexec_b64 s[8:9], s[0:1]
	s_cbranch_execnz .LBB3_38
	s_or_b64 exec, exec, s[8:9]
	s_and_saveexec_b64 s[8:9], s[2:3]
	s_cbranch_execnz .LBB3_39

.LBB3_33:
	s_waitcnt lgkmcnt(0)
	s_barrier
	s_add_i32 s60, s45, 16
	s_and_b32 s60, s60, 28
	s_or_b32 s60, s60, 2
	s_lshl_b32 s60, s60, 15
	s_or_b32 s61, s60, 0x4000
	s_mov_b32 m0, s38
	s_nop 0
	buffer_load_dwordx4 v166, s[12:15], s61 offen lds
	s_or_b32 s61, s60, 0x6000
	s_mov_b32 m0, s39
	s_nop 0
	buffer_load_dwordx4 v166, s[12:15], s61 offen lds
	s_or_b32 s61, s60, 0xc000
	s_mov_b32 m0, s40
	s_nop 0
	buffer_load_dwordx4 v166, s[12:15], s61 offen lds
	s_or_b32 s61, s60, 0xe000
	s_mov_b32 m0, s42
	s_nop 0
	buffer_load_dwordx4 v166, s[12:15], s61 offen lds
	s_lshr_b32 s62, s21, 1
	s_lshr_b32 s63, s20, 2
	s_xor_b32 s62, s62, s63
	s_and_b32 s62, s62, 1
	s_lshl_b32 s63, s62, 16
	v_add_u32_e32 v232, s63, v168
	v_add_u32_e32 v233, 0x8000, v232
	s_add_i32 s63, s45, 16
	s_and_b32 s63, s63, 28
	s_lshl_b32 s64, s62, 1
	s_or_b32 s63, s63, s64
	s_add_i32 s63, s63, s41
	s_lshl_b32 s63, s63, 1
	v_mov_b32_e32 v234, s63
	s_or_b32 s63, s63, 1
	v_mov_b32_e32 v235, s63
	s_lshl_b32 s64, s62, 8
	s_add_i32 s64, s64, s47
	s_add_i32 s64, s64, 0x20600
	v_lshl_add_u32 v236, v167, 2, s64
	s_waitcnt vmcnt(4)
	s_barrier
	ds_read_b128 v[144:147], v232 offset:0
	ds_read_b128 v[148:151], v232 offset:256
	ds_read_b128 v[152:155], v232 offset:2048
	ds_read_b128 v[156:159], v232 offset:2304
	ds_read_b128 v[224:227], v232 offset:4096
	s_waitcnt lgkmcnt(4)
	v_mfma_f32_16x16x32_bf16 v[208:211], v[0:3], v[144:147], 0
	v_mfma_f32_16x16x32_bf16 v[212:215], v[4:7], v[144:147], 0
	ds_read_b128 v[228:231], v232 offset:4352
	s_waitcnt lgkmcnt(4)
	v_mfma_f32_16x16x32_bf16 v[216:219], v[0:3], v[148:151], 0
	v_mfma_f32_16x16x32_bf16 v[220:223], v[4:7], v[148:151], 0
	ds_read_b128 v[144:147], v232 offset:6144
	s_waitcnt lgkmcnt(4)
	v_mfma_f32_16x16x32_bf16 v[208:211], v[8:11], v[152:155], v[208:211]
	v_mfma_f32_16x16x32_bf16 v[212:215], v[12:15], v[152:155], v[212:215]
	ds_read_b128 v[148:151], v232 offset:6400
	s_waitcnt lgkmcnt(4)
	v_mfma_f32_16x16x32_bf16 v[216:219], v[8:11], v[156:159], v[216:219]
	v_mfma_f32_16x16x32_bf16 v[220:223], v[12:15], v[156:159], v[220:223]
	ds_read_b128 v[152:155], v232 offset:8192
	s_waitcnt lgkmcnt(4)
	v_mfma_f32_16x16x32_bf16 v[208:211], v[16:19], v[224:227], v[208:211]
	v_mfma_f32_16x16x32_bf16 v[212:215], v[20:23], v[224:227], v[212:215]
	ds_read_b128 v[156:159], v232 offset:8448
	s_waitcnt lgkmcnt(4)
	v_mfma_f32_16x16x32_bf16 v[216:219], v[16:19], v[228:231], v[216:219]
	v_mfma_f32_16x16x32_bf16 v[220:223], v[20:23], v[228:231], v[220:223]
	ds_read_b128 v[224:227], v232 offset:10240
	s_waitcnt lgkmcnt(4)
	v_mfma_f32_16x16x32_bf16 v[208:211], v[24:27], v[144:147], v[208:211]
	v_mfma_f32_16x16x32_bf16 v[212:215], v[28:31], v[144:147], v[212:215]
	ds_read_b128 v[228:231], v232 offset:10496
	s_waitcnt lgkmcnt(4)
	v_mfma_f32_16x16x32_bf16 v[216:219], v[24:27], v[148:151], v[216:219]
	v_mfma_f32_16x16x32_bf16 v[220:223], v[28:31], v[148:151], v[220:223]
	ds_read_b128 v[144:147], v232 offset:12288
	s_waitcnt lgkmcnt(4)
	v_mfma_f32_16x16x32_bf16 v[208:211], v[32:35], v[152:155], v[208:211]
	v_mfma_f32_16x16x32_bf16 v[212:215], v[36:39], v[152:155], v[212:215]
	ds_read_b128 v[148:151], v232 offset:12544
	s_waitcnt lgkmcnt(4)
	v_mfma_f32_16x16x32_bf16 v[216:219], v[32:35], v[156:159], v[216:219]
	v_mfma_f32_16x16x32_bf16 v[220:223], v[36:39], v[156:159], v[220:223]
	ds_read_b128 v[152:155], v232 offset:14336
	s_waitcnt lgkmcnt(4)
	v_mfma_f32_16x16x32_bf16 v[208:211], v[40:43], v[224:227], v[208:211]
	v_mfma_f32_16x16x32_bf16 v[212:215], v[44:47], v[224:227], v[212:215]
	ds_read_b128 v[156:159], v232 offset:14592
	s_waitcnt lgkmcnt(4)
	v_mfma_f32_16x16x32_bf16 v[216:219], v[40:43], v[228:231], v[216:219]
	v_mfma_f32_16x16x32_bf16 v[220:223], v[44:47], v[228:231], v[220:223]
	s_waitcnt lgkmcnt(3)
	v_mfma_f32_16x16x32_bf16 v[208:211], v[48:51], v[144:147], v[208:211]
	v_mfma_f32_16x16x32_bf16 v[212:215], v[52:55], v[144:147], v[212:215]
	s_waitcnt lgkmcnt(2)
	v_mfma_f32_16x16x32_bf16 v[216:219], v[48:51], v[148:151], v[216:219]
	v_mfma_f32_16x16x32_bf16 v[220:223], v[52:55], v[148:151], v[220:223]
	s_waitcnt lgkmcnt(1)
	v_mfma_f32_16x16x32_bf16 v[208:211], v[56:59], v[152:155], v[208:211]
	v_mfma_f32_16x16x32_bf16 v[212:215], v[60:63], v[152:155], v[212:215]
	s_waitcnt lgkmcnt(0)
	v_mfma_f32_16x16x32_bf16 v[216:219], v[56:59], v[156:159], v[216:219]
	v_mfma_f32_16x16x32_bf16 v[220:223], v[60:63], v[156:159], v[220:223]
	s_waitcnt vmcnt(0)
	s_barrier
	ds_read_b128 v[144:147], v233 offset:0
	ds_read_b128 v[148:151], v233 offset:256
	ds_read_b128 v[152:155], v233 offset:2048
	ds_read_b128 v[156:159], v233 offset:2304
	ds_read_b128 v[224:227], v233 offset:4096
	s_waitcnt lgkmcnt(4)
	v_mfma_f32_16x16x32_bf16 v[208:211], v[64:67], v[144:147], v[208:211]
	v_mfma_f32_16x16x32_bf16 v[212:215], v[68:71], v[144:147], v[212:215]
	ds_read_b128 v[228:231], v233 offset:4352
	s_waitcnt lgkmcnt(4)
	v_mfma_f32_16x16x32_bf16 v[216:219], v[64:67], v[148:151], v[216:219]
	v_mfma_f32_16x16x32_bf16 v[220:223], v[68:71], v[148:151], v[220:223]
	ds_read_b128 v[144:147], v233 offset:6144
	s_waitcnt lgkmcnt(4)
	v_mfma_f32_16x16x32_bf16 v[208:211], v[72:75], v[152:155], v[208:211]
	v_mfma_f32_16x16x32_bf16 v[212:215], v[76:79], v[152:155], v[212:215]
	ds_read_b128 v[148:151], v233 offset:6400
	s_waitcnt lgkmcnt(4)
	v_mfma_f32_16x16x32_bf16 v[216:219], v[72:75], v[156:159], v[216:219]
	v_mfma_f32_16x16x32_bf16 v[220:223], v[76:79], v[156:159], v[220:223]
	ds_read_b128 v[152:155], v233 offset:8192
	s_waitcnt lgkmcnt(4)
	v_mfma_f32_16x16x32_bf16 v[208:211], v[80:83], v[224:227], v[208:211]
	v_mfma_f32_16x16x32_bf16 v[212:215], v[84:87], v[224:227], v[212:215]
	ds_read_b128 v[156:159], v233 offset:8448
	s_waitcnt lgkmcnt(4)
	v_mfma_f32_16x16x32_bf16 v[216:219], v[80:83], v[228:231], v[216:219]
	v_mfma_f32_16x16x32_bf16 v[220:223], v[84:87], v[228:231], v[220:223]
	ds_read_b128 v[224:227], v233 offset:10240
	s_waitcnt lgkmcnt(4)
	v_mfma_f32_16x16x32_bf16 v[208:211], v[88:91], v[144:147], v[208:211]
	v_mfma_f32_16x16x32_bf16 v[212:215], v[92:95], v[144:147], v[212:215]
	ds_read_b128 v[228:231], v233 offset:10496
	s_waitcnt lgkmcnt(4)
	v_mfma_f32_16x16x32_bf16 v[216:219], v[88:91], v[148:151], v[216:219]
	v_mfma_f32_16x16x32_bf16 v[220:223], v[92:95], v[148:151], v[220:223]
	ds_read_b128 v[144:147], v233 offset:12288
	s_waitcnt lgkmcnt(4)
	v_mfma_f32_16x16x32_bf16 v[208:211], v[96:99], v[152:155], v[208:211]
	v_mfma_f32_16x16x32_bf16 v[212:215], v[100:103], v[152:155], v[212:215]
	ds_read_b128 v[148:151], v233 offset:12544
	s_waitcnt lgkmcnt(4)
	v_mfma_f32_16x16x32_bf16 v[216:219], v[96:99], v[156:159], v[216:219]
	v_mfma_f32_16x16x32_bf16 v[220:223], v[100:103], v[156:159], v[220:223]
	ds_read_b128 v[152:155], v233 offset:14336
	s_waitcnt lgkmcnt(4)
	v_mfma_f32_16x16x32_bf16 v[208:211], v[104:107], v[224:227], v[208:211]
	v_mfma_f32_16x16x32_bf16 v[212:215], v[108:111], v[224:227], v[212:215]
	ds_read_b128 v[156:159], v233 offset:14592
	s_waitcnt lgkmcnt(4)
	v_mfma_f32_16x16x32_bf16 v[216:219], v[104:107], v[228:231], v[216:219]
	v_mfma_f32_16x16x32_bf16 v[220:223], v[108:111], v[228:231], v[220:223]
	s_waitcnt lgkmcnt(3)
	v_mfma_f32_16x16x32_bf16 v[208:211], v[112:115], v[144:147], v[208:211]
	v_mfma_f32_16x16x32_bf16 v[212:215], v[116:119], v[144:147], v[212:215]
	s_waitcnt lgkmcnt(2)
	v_mfma_f32_16x16x32_bf16 v[216:219], v[112:115], v[148:151], v[216:219]
	v_mfma_f32_16x16x32_bf16 v[220:223], v[116:119], v[148:151], v[220:223]
	s_waitcnt lgkmcnt(1)
	v_mfma_f32_16x16x32_bf16 v[208:211], v[120:123], v[152:155], v[208:211]
	v_mfma_f32_16x16x32_bf16 v[212:215], v[124:127], v[152:155], v[212:215]
	s_waitcnt lgkmcnt(0)
	v_mfma_f32_16x16x32_bf16 v[216:219], v[120:123], v[156:159], v[216:219]
	v_mfma_f32_16x16x32_bf16 v[220:223], v[124:127], v[156:159], v[220:223]
	s_movk_i32 s65, 0xffc0
	s_movk_i32 s66, 0xff80
	s_brev_b32 s67, -2
	s_nop 7
	s_nop 3
	v_and_or_b32 v237, v208, s65, v234
	v_and_or_b32 v238, v216, s65, v235
	v_max3_f32 v161, v161, v237, v238
	v_and_b32_e32 v174, 0xffffff80, v208
	v_and_b32_e32 v175, 0xffffff80, v216
	v_and_or_b32 v237, v209, s65, v234
	v_and_or_b32 v238, v217, s65, v235
	v_max3_f32 v160, v160, v237, v238
	v_and_or_b32 v237, v209, s66, 1
	v_and_or_b32 v238, v217, s66, 1
	v_max_f32_e32 v174, v174, v237
	v_max_f32_e32 v175, v175, v238
	v_and_or_b32 v237, v210, s65, v234
	v_and_or_b32 v238, v218, s65, v235
	v_max3_f32 v162, v162, v237, v238
	v_and_or_b32 v237, v210, s66, 2
	v_and_or_b32 v238, v218, s66, 2
	v_max_f32_e32 v174, v174, v237
	v_max_f32_e32 v175, v175, v238
	v_and_or_b32 v237, v211, s65, v234
	v_and_or_b32 v238, v219, s65, v235
	v_max3_f32 v163, v163, v237, v238
	v_and_or_b32 v237, v211, s66, 3
	v_and_or_b32 v238, v219, s66, 3
	v_max_f32_e32 v174, v174, v237
	v_max_f32_e32 v175, v175, v238
	v_and_or_b32 v237, v212, s65, v234
	v_and_or_b32 v238, v220, s65, v235
	v_max3_f32 v203, v203, v237, v238
	v_and_or_b32 v237, v212, s66, 4
	v_and_or_b32 v238, v220, s66, 4
	v_max_f32_e32 v174, v174, v237
	v_max_f32_e32 v175, v175, v238
	v_and_or_b32 v237, v213, s65, v234
	v_and_or_b32 v238, v221, s65, v235
	v_max3_f32 v204, v204, v237, v238
	v_and_or_b32 v237, v213, s66, 5
	v_and_or_b32 v238, v221, s66, 5
	v_max_f32_e32 v174, v174, v237
	v_max_f32_e32 v175, v175, v238
	v_and_or_b32 v237, v214, s65, v234
	v_and_or_b32 v238, v222, s65, v235
	v_max3_f32 v205, v205, v237, v238
	v_and_or_b32 v237, v214, s66, 6
	v_and_or_b32 v238, v222, s66, 6
	v_max_f32_e32 v174, v174, v237
	v_max_f32_e32 v175, v175, v238
	v_and_or_b32 v237, v215, s65, v234
	v_and_or_b32 v238, v223, s65, v235
	v_max3_f32 v206, v206, v237, v238
	v_and_or_b32 v237, v215, s66, 7
	v_and_or_b32 v238, v223, s66, 7
	v_max_f32_e32 v174, v174, v237
	v_max_f32_e32 v175, v175, v238
	v_or_b32_e32 v237, v173, v174
	v_ashrrev_i32_e32 v238, 31, v174
	v_bitop3_b32 v237, v238, v237, s67 bitop3:0x6c
	ds_max_i32 v236, v237
	v_or_b32_e32 v237, v173, v175
	v_ashrrev_i32_e32 v238, 31, v175
	v_bitop3_b32 v237, v238, v237, s67 bitop3:0x6c
	ds_max_i32 v236, v237 offset:64
	s_add_i32 s6, s24, -1
	s_add_i32 s0, s6, s22
	s_lshl_b32 s0, s0, 2
	s_and_b32 s0, s0, 28
	s_add_i32 s41, s41, s0
	s_lshl_b32 s0, s41, 1
	s_add_i32 s1, s0, 4
	s_add_i32 s0, s0, 5
	v_mov_b32_e32 v8, s0
	s_lshl_b32 s0, s24, 9
	s_add_i32 s0, s0, s47
	s_add_i32 s0, s0, 0x20000
	v_mov_b32_e32 v2, s1
	v_lshl_add_u32 v0, v167, 2, s0
	s_movk_i32 s0, 0xffc0
	v_add_u32_e32 v9, 0xfffffd00, v0
	v_and_or_b32 v0, v136, s0, v2
	v_and_or_b32 v1, v140, s0, v8
	v_max3_f32 v0, v161, v0, v1
	s_movk_i32 s2, 0xff80
	v_and_or_b32 v1, v137, s0, v2
	v_and_or_b32 v5, v141, s0, v8
	v_and_b32_e32 v3, 0xffffff80, v140
	v_and_b32_e32 v4, 0xffffff80, v136
	v_max3_f32 v1, v160, v1, v5
	v_and_or_b32 v5, v141, s2, 1
	v_and_or_b32 v6, v137, s2, 1
	v_max_f32 v4, v4, v6
	v_max_f32 v5, v3, v5
	v_and_or_b32 v3, v138, s0, v2
	v_and_or_b32 v6, v142, s0, v8
	v_max3_f32 v3, v162, v3, v6
	v_and_or_b32 v6, v142, s2, 2
	v_and_or_b32 v7, v138, s2, 2
	v_max_f32 v7, v4, v7
	v_max_f32 v5, v5, v6
	v_and_or_b32 v4, v139, s0, v2
	v_and_or_b32 v6, v143, s0, v8
	v_max3_f32 v4, v163, v4, v6
	v_and_or_b32 v6, v143, s2, 3
	v_and_or_b32 v10, v139, s2, 3
	v_max_f32 v7, v7, v10
	v_max_f32 v6, v5, v6
	v_and_or_b32 v5, v128, s0, v2
	v_and_or_b32 v10, v132, s0, v8
	v_max3_f32 v5, v203, v5, v10
	v_and_or_b32 v10, v132, s2, 4
	v_and_or_b32 v11, v128, s2, 4
	v_max_f32 v7, v7, v11
	v_max_f32 v10, v6, v10
	v_and_or_b32 v6, v129, s0, v2
	v_and_or_b32 v11, v133, s0, v8
	v_max3_f32 v6, v204, v6, v11
	v_and_or_b32 v11, v133, s2, 5
	v_and_or_b32 v12, v129, s2, 5
	v_max_f32 v12, v7, v12
	v_max_f32 v10, v10, v11
	v_and_or_b32 v7, v130, s0, v2
	v_and_or_b32 v11, v134, s0, v8
	v_max3_f32 v7, v205, v7, v11
	v_and_or_b32 v11, v134, s2, 6
	v_max_f32 v10, v10, v11
	v_and_or_b32 v2, v131, s0, v2
	v_and_or_b32 v8, v135, s0, v8
	v_and_or_b32 v11, v131, s2, 7
	v_and_or_b32 v13, v130, s2, 6
	v_max_f32 v12, v12, v13
	v_max3_f32 v8, v206, v2, v8
	v_and_or_b32 v2, v135, s2, 7
	v_max_f32 v11, v12, v11
	v_max_f32 v2, v10, v2
	s_brev_b32 s3, -2
	v_or_b32_e32 v10, v173, v11
	v_ashrrev_i32_e32 v11, 31, v11
	v_bitop3_b32 v10, v11, v10, s3 bitop3:0x6c
	ds_max_i32 v9, v10
	v_or_b32_e32 v10, v173, v2
	v_ashrrev_i32_e32 v2, 31, v2
	v_bitop3_b32 v2, v2, v10, s3 bitop3:0x6c
	ds_max_i32 v9, v2 offset:64
	v_mbcnt_lo_u32_b32 v2, -1, 0
	s_andn2_b32 s23, s23, 63
	s_lshl_b64 s[0:1], s[16:17], 13
	s_waitcnt vmcnt(0)
	v_mbcnt_hi_u32_b32 v2, -1, v2
	s_add_u32 s4, s10, s0
	v_add_u32_e32 v9, s23, v2
	s_addc_u32 s5, s11, s1
	s_mov_b32 s6, 4
	s_lshl_b32 s0, s6, 7
	v_cmp_gt_i32_e32 vcc, s0, v9
	s_waitcnt lgkmcnt(0)
	s_barrier
	s_and_saveexec_b64 s[0:1], vcc
	s_cbranch_execz .LBB3_35
	v_mov_b32_e32 v10, 0x20000
	v_lshl_add_u32 v10, v9, 2, v10
	ds_read_b32 v10, v10
	s_movk_i32 s6, 0x63
	v_and_b32_e32 v12, 0x7f, v9
	s_waitcnt lgkmcnt(0)
	v_ashrrev_i32_e32 v11, 31, v10
	v_and_b32_e32 v13, 0x7fffffff, v11
	v_bitop3_b32 v11, v11, v10, s3 bitop3:0x6c
	v_lshlrev_b32_e32 v14, 2, v11
	v_and_b32_e32 v14, 16, v14
	s_lshl_b32 s3, s20, 7
	v_bitop3_b32 v13, v13, s6, v10 bitop3:0x48
	v_or3_b32 v13, v13, s3, v14
	v_bfrev_b32_e32 v14, 1
	v_cmp_lt_i32_e32 vcc, -1, v10
	v_lshrrev_b32_e32 v15, 1, v11
	v_and_b32_e32 v15, 12, v15
	v_cndmask_b32_e32 v10, -1, v14, vcc
	v_bitop3_b32 v11, v11, v10, s2 bitop3:0x6c
	s_movk_i32 s2, 0x3ff
	v_bitop3_b32 v10, v13, s2, v15 bitop3:0x36
	s_lshl_b32 s2, s22, 7
	s_addk_i32 s2, 0x80
	v_add_u32_e32 v9, s2, v9
	s_movk_i32 s2, 0x380
	v_and_or_b32 v9, v9, s2, v12
	v_lshlrev_b32_e32 v9, 3, v9
	global_atomic_umax_x2 v9, v[10:11], s[4:5]
